# GEMM epilogues of P6/P9/P15: all per-row ss/rs loads of a unit requested up front with counted waits (was one load + vmcnt(0) per row group); plus P2 changes
# baseline (speedup 1.0000x reference)
.LBB0_474:
	v_lshl_add_u32 v152, s24, 8, v156
	v_ashrrev_i32_e32 v153, 31, v152
	v_lshl_add_u64 v[154:155], v[152:153], 3, s[10:11]
	global_load_dwordx2 v[166:167], v[154:155], off
	global_load_dwordx2 v[178:179], v[154:155], off offset:128
	global_load_dwordx2 v[180:181], v[154:155], off offset:256
	global_load_dwordx2 v[182:183], v[154:155], off offset:384
	global_load_dwordx2 v[184:185], v[154:155], off offset:1024
	global_load_dwordx2 v[186:187], v[154:155], off offset:1152
	global_load_dwordx2 v[188:189], v[154:155], off offset:1280
	global_load_dwordx2 v[190:191], v[154:155], off offset:1408
	v_pk_mul_f32 v[126:127], v[118:119], v[126:127]
	v_pk_mul_f32 v[122:123], v[114:115], v[122:123]
	v_pk_mul_f32 v[128:129], v[120:121], v[128:129]
	v_pk_mul_f32 v[124:125], v[116:117], v[124:125]
	v_mov_b32_e32 v168, 0
	v_mov_b32_e32 v169, 0
	v_lshl_or_b32 v148, s54, 7, v159
	v_mov_b64_e32 v[150:151], s[8:9]
	v_or_b32_e32 v170, 16, v152
	v_ashrrev_i32_e32 v171, 31, v170
	v_pk_mul_f32 v[110:111], v[102:103], v[110:111]
	v_pk_mul_f32 v[106:107], v[98:99], v[106:107]
	v_pk_mul_f32 v[112:113], v[104:105], v[112:113]
	v_pk_mul_f32 v[108:109], v[100:101], v[108:109]
	v_pk_mul_f32 v[94:95], v[86:87], v[94:95]
	v_pk_mul_f32 v[90:91], v[82:83], v[90:91]
	v_pk_mul_f32 v[96:97], v[88:89], v[96:97]
	v_pk_mul_f32 v[92:93], v[84:85], v[92:93]
	v_pk_mul_f32 v[78:79], v[74:75], v[78:79]
	v_pk_mul_f32 v[66:67], v[70:71], v[66:67]
	v_pk_mul_f32 v[80:81], v[76:77], v[80:81]
	v_pk_mul_f32 v[68:69], v[72:73], v[68:69]
	v_pk_mul_f32 v[62:63], v[58:59], v[62:63]
	v_pk_mul_f32 v[50:51], v[54:55], v[50:51]
	v_pk_mul_f32 v[64:65], v[60:61], v[64:65]
	v_pk_mul_f32 v[52:53], v[56:57], v[52:53]
	v_pk_mul_f32 v[46:47], v[42:43], v[46:47]
	v_pk_mul_f32 v[34:35], v[38:39], v[34:35]
	v_pk_mul_f32 v[48:49], v[44:45], v[48:49]
	v_pk_mul_f32 v[36:37], v[40:41], v[36:37]
	v_pk_mul_f32 v[30:31], v[26:27], v[30:31]
	v_pk_mul_f32 v[18:19], v[22:23], v[18:19]
	v_pk_mul_f32 v[32:33], v[28:29], v[32:33]
	v_pk_mul_f32 v[20:21], v[24:25], v[20:21]
	v_pk_mul_f32 v[14:15], v[6:7], v[14:15]
	v_pk_mul_f32 v[10:11], v[2:3], v[10:11]
	v_pk_mul_f32 v[16:17], v[8:9], v[16:17]
	v_pk_mul_f32 v[12:13], v[4:5], v[12:13]
	s_andn2_b64 vcc, exec, s[4:5]
	s_mov_b64 s[4:5], -1
	s_waitcnt vmcnt(7)
	v_ffbh_u32_e32 v149, v167
	v_min_u32_e32 v153, 32, v149
	v_lshlrev_b64 v[166:167], v153, v[166:167]
	v_min_u32_e32 v149, 1, v166
	v_or_b32_e32 v149, v167, v149
	v_cvt_f32_u32_e32 v165, v149
	v_sub_u32_e32 v153, 32, v153
	v_ashrrev_i32_e32 v149, 31, v148
	v_mad_i64_i32 v[166:167], s[26:27], v152, s48, v[150:151]
	v_ldexp_f32 v153, v165, v153
	v_fmamk_f32 v153, v153, 0x30000000, v163
	v_rsq_f32_e32 v165, v153
	v_mul_f32_e32 v172, 0x3e000000, v153
	v_mul_f32_e32 v174, 0xbfb8aa3b, v165
	v_pk_mul_f32 v[118:119], v[118:119], v[174:175] op_sel_hi:[1,0]
	v_pk_mul_f32 v[114:115], v[114:115], v[174:175] op_sel_hi:[1,0]
	v_exp_f32_e32 v118, v118
	v_exp_f32_e32 v119, v119
	v_exp_f32_e32 v114, v114
	v_exp_f32_e32 v115, v115
	v_pk_mul_f32 v[120:121], v[120:121], v[174:175] op_sel_hi:[1,0]
	v_pk_mul_f32 v[116:117], v[116:117], v[174:175] op_sel_hi:[1,0]
	v_exp_f32_e32 v120, v120
	v_exp_f32_e32 v121, v121
	v_exp_f32_e32 v116, v116
	v_exp_f32_e32 v117, v117
	v_pk_fma_f32 v[118:119], v[172:173], v[118:119], v[172:173] op_sel_hi:[0,1,0]
	v_pk_fma_f32 v[114:115], v[172:173], v[114:115], v[172:173] op_sel_hi:[0,1,0]
	v_rcp_f32_e32 v118, v118
	v_rcp_f32_e32 v119, v119
	v_rcp_f32_e32 v114, v114
	v_rcp_f32_e32 v115, v115
	v_pk_fma_f32 v[120:121], v[172:173], v[120:121], v[172:173] op_sel_hi:[0,1,0]
	v_pk_fma_f32 v[116:117], v[172:173], v[116:117], v[172:173] op_sel_hi:[0,1,0]
	v_rcp_f32_e32 v120, v120
	v_rcp_f32_e32 v121, v121
	v_rcp_f32_e32 v116, v116
	v_rcp_f32_e32 v117, v117
	v_pk_mul_f32 v[118:119], v[126:127], v[118:119]
	v_pk_mul_f32 v[114:115], v[122:123], v[114:115]
	v_med3_f32 v118, v118, s49, v164
	v_med3_f32 v119, v119, s49, v164
	v_med3_f32 v114, v114, s49, v164
	v_med3_f32 v115, v115, s49, v164
	v_cvt_pk_fp8_f32 v168, v118, v119
	v_cvt_pk_fp8_f32 v169, v114, v115
	v_pk_mul_f32 v[120:121], v[128:129], v[120:121]
	v_pk_mul_f32 v[116:117], v[124:125], v[116:117]
	v_med3_f32 v120, v120, s49, v164
	v_med3_f32 v121, v121, s49, v164
	v_med3_f32 v114, v116, s49, v164
	v_med3_f32 v115, v117, s49, v164
	v_cvt_pk_fp8_f32 v168, v120, v121 op_sel:[0,0,1]
	v_cvt_pk_fp8_f32 v169, v114, v115 op_sel:[0,0,1]
	v_lshl_add_u64 v[114:115], v[166:167], 0, v[148:149]
	v_lshl_add_u64 v[116:117], v[170:171], 3, s[10:11]
	global_store_dwordx2 v[114:115], v[168:169], off
	s_nop 0
	v_mov_b32_e32 v116, 0
	s_waitcnt vmcnt(7)
	v_mov_b32_e32 v114, v178
	v_mov_b32_e32 v115, v179
	v_ffbh_u32_e32 v117, v115
	v_min_u32_e32 v118, 32, v117
	v_lshlrev_b64 v[114:115], v118, v[114:115]
	v_min_u32_e32 v114, 1, v114
	v_or_b32_e32 v114, v115, v114
	v_cvt_f32_u32_e32 v115, v114
	v_sub_u32_e32 v118, 32, v118
	v_mov_b32_e32 v117, 0
	v_or_b32_e32 v114, 32, v152
	v_ldexp_f32 v115, v115, v118
	v_fmamk_f32 v115, v115, 0x30000000, v163
	v_rsq_f32_e32 v121, v115
	v_mul_f32_e32 v120, 0x3e000000, v115
	v_mad_i64_i32 v[118:119], s[26:27], v170, s48, v[150:151]
	v_mul_f32_e32 v122, 0xbfb8aa3b, v121
	v_pk_mul_f32 v[102:103], v[102:103], v[122:123] op_sel_hi:[1,0]
	v_pk_mul_f32 v[98:99], v[98:99], v[122:123] op_sel_hi:[1,0]
	v_exp_f32_e32 v102, v102
	v_exp_f32_e32 v103, v103
	v_exp_f32_e32 v98, v98
	v_exp_f32_e32 v99, v99
	v_pk_mul_f32 v[104:105], v[104:105], v[122:123] op_sel_hi:[1,0]
	v_pk_mul_f32 v[100:101], v[100:101], v[122:123] op_sel_hi:[1,0]
	v_exp_f32_e32 v104, v104
	v_exp_f32_e32 v105, v105
	v_exp_f32_e32 v100, v100
	v_exp_f32_e32 v101, v101
	v_pk_fma_f32 v[102:103], v[120:121], v[102:103], v[120:121] op_sel_hi:[0,1,0]
	v_pk_fma_f32 v[98:99], v[120:121], v[98:99], v[120:121] op_sel_hi:[0,1,0]
	v_rcp_f32_e32 v102, v102
	v_rcp_f32_e32 v103, v103
	v_rcp_f32_e32 v98, v98
	v_rcp_f32_e32 v99, v99
	v_pk_fma_f32 v[104:105], v[120:121], v[104:105], v[120:121] op_sel_hi:[0,1,0]
	v_pk_fma_f32 v[100:101], v[120:121], v[100:101], v[120:121] op_sel_hi:[0,1,0]
	v_rcp_f32_e32 v104, v104
	v_rcp_f32_e32 v105, v105
	v_rcp_f32_e32 v100, v100
	v_rcp_f32_e32 v101, v101
	v_pk_mul_f32 v[102:103], v[110:111], v[102:103]
	v_pk_mul_f32 v[98:99], v[106:107], v[98:99]
	v_med3_f32 v102, v102, s49, v164
	v_med3_f32 v103, v103, s49, v164
	v_med3_f32 v98, v98, s49, v164
	v_med3_f32 v99, v99, s49, v164
	v_cvt_pk_fp8_f32 v116, v102, v103
	v_cvt_pk_fp8_f32 v117, v98, v99
	v_pk_mul_f32 v[104:105], v[112:113], v[104:105]
	v_pk_mul_f32 v[100:101], v[108:109], v[100:101]
	v_med3_f32 v104, v104, s49, v164
	v_med3_f32 v105, v105, s49, v164
	v_med3_f32 v98, v100, s49, v164
	v_med3_f32 v99, v101, s49, v164
	v_cvt_pk_fp8_f32 v116, v104, v105 op_sel:[0,0,1]
	v_cvt_pk_fp8_f32 v117, v98, v99 op_sel:[0,0,1]
	v_ashrrev_i32_e32 v115, 31, v114
	v_lshl_add_u64 v[98:99], v[118:119], 0, v[148:149]
	v_lshl_add_u64 v[100:101], v[114:115], 3, s[10:11]
	global_store_dwordx2 v[98:99], v[116:117], off
	s_nop 0
	v_mov_b32_e32 v100, 0
	s_waitcnt vmcnt(7)
	v_mov_b32_e32 v98, v180
	v_mov_b32_e32 v99, v181
	v_ffbh_u32_e32 v101, v99
	v_min_u32_e32 v102, 32, v101
	v_lshlrev_b64 v[98:99], v102, v[98:99]
	v_min_u32_e32 v98, 1, v98
	v_or_b32_e32 v98, v99, v98
	v_cvt_f32_u32_e32 v99, v98
	v_sub_u32_e32 v102, 32, v102
	v_mov_b32_e32 v101, 0
	v_or_b32_e32 v98, 48, v152
	v_ldexp_f32 v99, v99, v102
	v_fmamk_f32 v99, v99, 0x30000000, v163
	v_rsq_f32_e32 v105, v99
	v_mul_f32_e32 v104, 0x3e000000, v99
	v_mad_i64_i32 v[102:103], s[26:27], v114, s48, v[150:151]
	v_mul_f32_e32 v106, 0xbfb8aa3b, v105
	v_pk_mul_f32 v[86:87], v[86:87], v[106:107] op_sel_hi:[1,0]
	v_pk_mul_f32 v[82:83], v[82:83], v[106:107] op_sel_hi:[1,0]
	v_exp_f32_e32 v86, v86
	v_exp_f32_e32 v87, v87
	v_exp_f32_e32 v82, v82
	v_exp_f32_e32 v83, v83
	v_pk_mul_f32 v[88:89], v[88:89], v[106:107] op_sel_hi:[1,0]
	v_pk_mul_f32 v[84:85], v[84:85], v[106:107] op_sel_hi:[1,0]
	v_exp_f32_e32 v88, v88
	v_exp_f32_e32 v89, v89
	v_exp_f32_e32 v84, v84
	v_exp_f32_e32 v85, v85
	v_pk_fma_f32 v[86:87], v[104:105], v[86:87], v[104:105] op_sel_hi:[0,1,0]
	v_pk_fma_f32 v[82:83], v[104:105], v[82:83], v[104:105] op_sel_hi:[0,1,0]
	v_rcp_f32_e32 v86, v86
	v_rcp_f32_e32 v87, v87
	v_rcp_f32_e32 v82, v82
	v_rcp_f32_e32 v83, v83
	v_pk_fma_f32 v[88:89], v[104:105], v[88:89], v[104:105] op_sel_hi:[0,1,0]
	v_pk_fma_f32 v[84:85], v[104:105], v[84:85], v[104:105] op_sel_hi:[0,1,0]
	v_rcp_f32_e32 v88, v88
	v_rcp_f32_e32 v89, v89
	v_rcp_f32_e32 v84, v84
	v_rcp_f32_e32 v85, v85
	v_pk_mul_f32 v[86:87], v[94:95], v[86:87]
	v_pk_mul_f32 v[82:83], v[90:91], v[82:83]
	v_med3_f32 v86, v86, s49, v164
	v_med3_f32 v87, v87, s49, v164
	v_med3_f32 v82, v82, s49, v164
	v_med3_f32 v83, v83, s49, v164
	v_cvt_pk_fp8_f32 v100, v86, v87
	v_cvt_pk_fp8_f32 v101, v82, v83
	v_pk_mul_f32 v[88:89], v[96:97], v[88:89]
	v_pk_mul_f32 v[84:85], v[92:93], v[84:85]
	v_med3_f32 v88, v88, s49, v164
	v_med3_f32 v89, v89, s49, v164
	v_med3_f32 v82, v84, s49, v164
	v_med3_f32 v83, v85, s49, v164
	v_cvt_pk_fp8_f32 v100, v88, v89 op_sel:[0,0,1]
	v_cvt_pk_fp8_f32 v101, v82, v83 op_sel:[0,0,1]
	v_ashrrev_i32_e32 v99, 31, v98
	v_lshl_add_u64 v[82:83], v[102:103], 0, v[148:149]
	v_lshl_add_u64 v[84:85], v[98:99], 3, s[10:11]
	global_store_dwordx2 v[82:83], v[100:101], off
	s_nop 0
	s_waitcnt vmcnt(7)
	v_mov_b32_e32 v82, v182
	v_mov_b32_e32 v83, v183
	v_ffbh_u32_e32 v84, v83
	v_min_u32_e32 v84, 32, v84
	v_lshlrev_b64 v[82:83], v84, v[82:83]
	v_min_u32_e32 v82, 1, v82
	v_or_b32_e32 v82, v83, v82
	v_cvt_f32_u32_e32 v82, v82
	v_sub_u32_e32 v83, 32, v84
	v_ldexp_f32 v82, v82, v83
	v_fmamk_f32 v84, v82, 0x30000000, v163
	v_rsq_f32_e32 v85, v84
	v_mul_f32_e32 v84, 0x3e000000, v84
	v_mov_b32_e32 v82, 0
	v_mov_b32_e32 v83, 0
	v_mul_f32_e32 v86, 0xbfb8aa3b, v85
	v_pk_mul_f32 v[74:75], v[74:75], v[86:87] op_sel_hi:[1,0]
	v_pk_mul_f32 v[70:71], v[70:71], v[86:87] op_sel_hi:[1,0]
	v_exp_f32_e32 v74, v74
	v_exp_f32_e32 v75, v75
	v_exp_f32_e32 v70, v70
	v_exp_f32_e32 v71, v71
	v_pk_mul_f32 v[76:77], v[76:77], v[86:87] op_sel_hi:[1,0]
	v_pk_mul_f32 v[72:73], v[72:73], v[86:87] op_sel_hi:[1,0]
	v_exp_f32_e32 v76, v76
	v_exp_f32_e32 v77, v77
	v_exp_f32_e32 v72, v72
	v_exp_f32_e32 v73, v73
	v_pk_fma_f32 v[74:75], v[84:85], v[74:75], v[84:85] op_sel_hi:[0,1,0]
	v_pk_fma_f32 v[70:71], v[84:85], v[70:71], v[84:85] op_sel_hi:[0,1,0]
	v_rcp_f32_e32 v74, v74
	v_rcp_f32_e32 v75, v75
	v_rcp_f32_e32 v70, v70
	v_rcp_f32_e32 v71, v71
	v_pk_fma_f32 v[76:77], v[84:85], v[76:77], v[84:85] op_sel_hi:[0,1,0]
	v_pk_fma_f32 v[72:73], v[84:85], v[72:73], v[84:85] op_sel_hi:[0,1,0]
	v_rcp_f32_e32 v76, v76
	v_rcp_f32_e32 v77, v77
	v_rcp_f32_e32 v72, v72
	v_rcp_f32_e32 v73, v73
	v_pk_mul_f32 v[74:75], v[78:79], v[74:75]
	v_pk_mul_f32 v[66:67], v[66:67], v[70:71]
	v_med3_f32 v70, v74, s49, v164
	v_med3_f32 v71, v75, s49, v164
	v_med3_f32 v66, v66, s49, v164
	v_med3_f32 v67, v67, s49, v164
	v_cvt_pk_fp8_f32 v82, v70, v71
	v_cvt_pk_fp8_f32 v83, v66, v67
	v_pk_mul_f32 v[76:77], v[80:81], v[76:77]
	v_pk_mul_f32 v[68:69], v[68:69], v[72:73]
	v_med3_f32 v72, v76, s49, v164
	v_med3_f32 v73, v77, s49, v164
	v_med3_f32 v66, v68, s49, v164
	v_med3_f32 v67, v69, s49, v164
	v_cvt_pk_fp8_f32 v82, v72, v73 op_sel:[0,0,1]
	v_cvt_pk_fp8_f32 v83, v66, v67 op_sel:[0,0,1]
	v_mad_i64_i32 v[66:67], s[26:27], v98, s48, v[150:151]
	v_lshl_add_u64 v[66:67], v[66:67], 0, v[148:149]
	global_store_dwordx2 v[66:67], v[82:83], off
	s_nop 0
	v_add_u32_e32 v71, 0x80, v152
	s_waitcnt vmcnt(7)
	v_mov_b32_e32 v66, v184
	v_mov_b32_e32 v67, v185
	v_ffbh_u32_e32 v68, v67
	v_min_u32_e32 v68, 32, v68
	v_lshlrev_b64 v[66:67], v68, v[66:67]
	v_min_u32_e32 v66, 1, v66
	v_or_b32_e32 v66, v67, v66
	v_cvt_f32_u32_e32 v67, v66
	v_sub_u32_e32 v68, 32, v68
	v_mov_b32_e32 v66, 0
	v_ldexp_f32 v67, v67, v68
	v_fmamk_f32 v68, v67, 0x30000000, v163
	v_rsq_f32_e32 v69, v68
	v_mul_f32_e32 v68, 0x3e000000, v68
	v_mov_b32_e32 v67, 0
	v_mul_f32_e32 v70, 0xbfb8aa3b, v69
	v_pk_mul_f32 v[58:59], v[58:59], v[70:71] op_sel_hi:[1,0]
	v_pk_mul_f32 v[54:55], v[54:55], v[70:71] op_sel_hi:[1,0]
	v_exp_f32_e32 v58, v58
	v_exp_f32_e32 v59, v59
	v_exp_f32_e32 v54, v54
	v_exp_f32_e32 v55, v55
	v_pk_mul_f32 v[60:61], v[60:61], v[70:71] op_sel_hi:[1,0]
	v_pk_mul_f32 v[56:57], v[56:57], v[70:71] op_sel_hi:[1,0]
	v_exp_f32_e32 v60, v60
	v_exp_f32_e32 v61, v61
	v_exp_f32_e32 v56, v56
	v_exp_f32_e32 v57, v57
	v_pk_fma_f32 v[58:59], v[68:69], v[58:59], v[68:69] op_sel_hi:[0,1,0]
	v_pk_fma_f32 v[54:55], v[68:69], v[54:55], v[68:69] op_sel_hi:[0,1,0]
	v_rcp_f32_e32 v58, v58
	v_rcp_f32_e32 v59, v59
	v_rcp_f32_e32 v54, v54
	v_rcp_f32_e32 v55, v55
	v_pk_fma_f32 v[60:61], v[68:69], v[60:61], v[68:69] op_sel_hi:[0,1,0]
	v_pk_fma_f32 v[56:57], v[68:69], v[56:57], v[68:69] op_sel_hi:[0,1,0]
	v_rcp_f32_e32 v60, v60
	v_rcp_f32_e32 v61, v61
	v_rcp_f32_e32 v56, v56
	v_rcp_f32_e32 v57, v57
	v_pk_mul_f32 v[58:59], v[62:63], v[58:59]
	v_pk_mul_f32 v[50:51], v[50:51], v[54:55]
	v_med3_f32 v54, v58, s49, v164
	v_med3_f32 v55, v59, s49, v164
	v_med3_f32 v50, v50, s49, v164
	v_med3_f32 v51, v51, s49, v164
	v_cvt_pk_fp8_f32 v66, v54, v55
	v_cvt_pk_fp8_f32 v67, v50, v51
	v_pk_mul_f32 v[60:61], v[64:65], v[60:61]
	v_pk_mul_f32 v[52:53], v[52:53], v[56:57]
	v_med3_f32 v56, v60, s49, v164
	v_med3_f32 v57, v61, s49, v164
	v_med3_f32 v50, v52, s49, v164
	v_med3_f32 v51, v53, s49, v164
	v_cvt_pk_fp8_f32 v66, v56, v57 op_sel:[0,0,1]
	v_cvt_pk_fp8_f32 v67, v50, v51 op_sel:[0,0,1]
	v_mad_i64_i32 v[50:51], s[26:27], v71, s48, v[150:151]
	v_lshl_add_u64 v[50:51], v[50:51], 0, v[148:149]
	global_store_dwordx2 v[50:51], v[66:67], off
	s_nop 0
	v_add_u32_e32 v55, 0x90, v152
	s_waitcnt vmcnt(7)
	v_mov_b32_e32 v50, v186
	v_mov_b32_e32 v51, v187
	v_ffbh_u32_e32 v52, v51
	v_min_u32_e32 v52, 32, v52
	v_lshlrev_b64 v[50:51], v52, v[50:51]
	v_min_u32_e32 v50, 1, v50
	v_or_b32_e32 v50, v51, v50
	v_cvt_f32_u32_e32 v51, v50
	v_sub_u32_e32 v52, 32, v52
	v_mov_b32_e32 v50, 0
	v_ldexp_f32 v51, v51, v52
	v_fmamk_f32 v52, v51, 0x30000000, v163
	v_rsq_f32_e32 v53, v52
	v_mul_f32_e32 v52, 0x3e000000, v52
	v_mov_b32_e32 v51, 0
	v_mul_f32_e32 v54, 0xbfb8aa3b, v53
	v_pk_mul_f32 v[42:43], v[42:43], v[54:55] op_sel_hi:[1,0]
	v_pk_mul_f32 v[38:39], v[38:39], v[54:55] op_sel_hi:[1,0]
	v_exp_f32_e32 v42, v42
	v_exp_f32_e32 v43, v43
	v_exp_f32_e32 v38, v38
	v_exp_f32_e32 v39, v39
	v_pk_mul_f32 v[44:45], v[44:45], v[54:55] op_sel_hi:[1,0]
	v_pk_mul_f32 v[40:41], v[40:41], v[54:55] op_sel_hi:[1,0]
	v_exp_f32_e32 v44, v44
	v_exp_f32_e32 v45, v45
	v_exp_f32_e32 v40, v40
	v_exp_f32_e32 v41, v41
	v_pk_fma_f32 v[42:43], v[52:53], v[42:43], v[52:53] op_sel_hi:[0,1,0]
	v_pk_fma_f32 v[38:39], v[52:53], v[38:39], v[52:53] op_sel_hi:[0,1,0]
	v_rcp_f32_e32 v42, v42
	v_rcp_f32_e32 v43, v43
	v_rcp_f32_e32 v38, v38
	v_rcp_f32_e32 v39, v39
	v_pk_fma_f32 v[44:45], v[52:53], v[44:45], v[52:53] op_sel_hi:[0,1,0]
	v_pk_fma_f32 v[40:41], v[52:53], v[40:41], v[52:53] op_sel_hi:[0,1,0]
	v_rcp_f32_e32 v44, v44
	v_rcp_f32_e32 v45, v45
	v_rcp_f32_e32 v40, v40
	v_rcp_f32_e32 v41, v41
	v_pk_mul_f32 v[42:43], v[46:47], v[42:43]
	v_pk_mul_f32 v[34:35], v[34:35], v[38:39]
	v_med3_f32 v38, v42, s49, v164
	v_med3_f32 v39, v43, s49, v164
	v_med3_f32 v34, v34, s49, v164
	v_med3_f32 v35, v35, s49, v164
	v_cvt_pk_fp8_f32 v50, v38, v39
	v_cvt_pk_fp8_f32 v51, v34, v35
	v_pk_mul_f32 v[44:45], v[48:49], v[44:45]
	v_pk_mul_f32 v[36:37], v[36:37], v[40:41]
	v_med3_f32 v40, v44, s49, v164
	v_med3_f32 v41, v45, s49, v164
	v_med3_f32 v34, v36, s49, v164
	v_med3_f32 v35, v37, s49, v164
	v_cvt_pk_fp8_f32 v50, v40, v41 op_sel:[0,0,1]
	v_cvt_pk_fp8_f32 v51, v34, v35 op_sel:[0,0,1]
	v_mad_i64_i32 v[34:35], s[26:27], v55, s48, v[150:151]
	v_lshl_add_u64 v[34:35], v[34:35], 0, v[148:149]
	global_store_dwordx2 v[34:35], v[50:51], off
	s_nop 0
	v_add_u32_e32 v39, 0xa0, v152
	s_waitcnt vmcnt(7)
	v_mov_b32_e32 v34, v188
	v_mov_b32_e32 v35, v189
	v_ffbh_u32_e32 v36, v35
	v_min_u32_e32 v36, 32, v36
	v_lshlrev_b64 v[34:35], v36, v[34:35]
	v_min_u32_e32 v34, 1, v34
	v_or_b32_e32 v34, v35, v34
	v_cvt_f32_u32_e32 v35, v34
	v_sub_u32_e32 v36, 32, v36
	v_mov_b32_e32 v34, 0
	v_ldexp_f32 v35, v35, v36
	v_fmamk_f32 v36, v35, 0x30000000, v163
	v_rsq_f32_e32 v37, v36
	v_mul_f32_e32 v36, 0x3e000000, v36
	v_mov_b32_e32 v35, 0
	v_mul_f32_e32 v38, 0xbfb8aa3b, v37
	v_pk_mul_f32 v[26:27], v[26:27], v[38:39] op_sel_hi:[1,0]
	v_pk_mul_f32 v[22:23], v[22:23], v[38:39] op_sel_hi:[1,0]
	v_exp_f32_e32 v26, v26
	v_exp_f32_e32 v27, v27
	v_exp_f32_e32 v22, v22
	v_exp_f32_e32 v23, v23
	v_pk_mul_f32 v[28:29], v[28:29], v[38:39] op_sel_hi:[1,0]
	v_pk_mul_f32 v[24:25], v[24:25], v[38:39] op_sel_hi:[1,0]
	v_exp_f32_e32 v28, v28
	v_exp_f32_e32 v29, v29
	v_exp_f32_e32 v24, v24
	v_exp_f32_e32 v25, v25
	v_pk_fma_f32 v[26:27], v[36:37], v[26:27], v[36:37] op_sel_hi:[0,1,0]
	v_pk_fma_f32 v[22:23], v[36:37], v[22:23], v[36:37] op_sel_hi:[0,1,0]
	v_rcp_f32_e32 v26, v26
	v_rcp_f32_e32 v27, v27
	v_rcp_f32_e32 v22, v22
	v_rcp_f32_e32 v23, v23
	v_pk_fma_f32 v[28:29], v[36:37], v[28:29], v[36:37] op_sel_hi:[0,1,0]
	v_pk_fma_f32 v[24:25], v[36:37], v[24:25], v[36:37] op_sel_hi:[0,1,0]
	v_rcp_f32_e32 v28, v28
	v_rcp_f32_e32 v29, v29
	v_rcp_f32_e32 v24, v24
	v_rcp_f32_e32 v25, v25
	v_pk_mul_f32 v[26:27], v[30:31], v[26:27]
	v_pk_mul_f32 v[18:19], v[18:19], v[22:23]
	v_med3_f32 v22, v26, s49, v164
	v_med3_f32 v23, v27, s49, v164
	v_med3_f32 v18, v18, s49, v164
	v_med3_f32 v19, v19, s49, v164
	v_cvt_pk_fp8_f32 v34, v22, v23
	v_cvt_pk_fp8_f32 v35, v18, v19
	v_pk_mul_f32 v[28:29], v[32:33], v[28:29]
	v_pk_mul_f32 v[20:21], v[20:21], v[24:25]
	v_med3_f32 v24, v28, s49, v164
	v_med3_f32 v25, v29, s49, v164
	v_med3_f32 v18, v20, s49, v164
	v_med3_f32 v19, v21, s49, v164
	v_cvt_pk_fp8_f32 v34, v24, v25 op_sel:[0,0,1]
	v_cvt_pk_fp8_f32 v35, v18, v19 op_sel:[0,0,1]
	v_mad_i64_i32 v[18:19], s[26:27], v39, s48, v[150:151]
	v_lshl_add_u64 v[18:19], v[18:19], 0, v[148:149]
	global_store_dwordx2 v[18:19], v[34:35], off
	s_nop 0
	v_add_u32_e32 v23, 0xb0, v152
	v_mov_b32_e32 v20, 0
	s_waitcnt vmcnt(7)
	v_mov_b32_e32 v18, v190
	v_mov_b32_e32 v19, v191
	v_ffbh_u32_e32 v21, v19
	v_min_u32_e32 v22, 32, v21
	v_lshlrev_b64 v[18:19], v22, v[18:19]
	v_min_u32_e32 v18, 1, v18
	v_or_b32_e32 v18, v19, v18
	v_cvt_f32_u32_e32 v18, v18
	v_sub_u32_e32 v19, 32, v22
	v_mov_b32_e32 v21, 0
	v_ldexp_f32 v18, v18, v19
	v_fmamk_f32 v18, v18, 0x30000000, v163
	v_rsq_f32_e32 v19, v18
	v_mul_f32_e32 v18, 0x3e000000, v18
	v_mul_f32_e32 v22, 0xbfb8aa3b, v19
	v_pk_mul_f32 v[6:7], v[6:7], v[22:23] op_sel_hi:[1,0]
	v_pk_mul_f32 v[2:3], v[2:3], v[22:23] op_sel_hi:[1,0]
	v_exp_f32_e32 v6, v6
	v_exp_f32_e32 v7, v7
	v_exp_f32_e32 v2, v2
	v_exp_f32_e32 v3, v3
	v_pk_mul_f32 v[8:9], v[8:9], v[22:23] op_sel_hi:[1,0]
	v_pk_mul_f32 v[4:5], v[4:5], v[22:23] op_sel_hi:[1,0]
	v_exp_f32_e32 v8, v8
	v_exp_f32_e32 v9, v9
	v_exp_f32_e32 v4, v4
	v_exp_f32_e32 v5, v5
	v_pk_fma_f32 v[6:7], v[18:19], v[6:7], v[18:19] op_sel_hi:[0,1,0]
	v_pk_fma_f32 v[2:3], v[18:19], v[2:3], v[18:19] op_sel_hi:[0,1,0]
	v_rcp_f32_e32 v6, v6
	v_rcp_f32_e32 v7, v7
	v_rcp_f32_e32 v2, v2
	v_rcp_f32_e32 v3, v3
	v_pk_fma_f32 v[8:9], v[18:19], v[8:9], v[18:19] op_sel_hi:[0,1,0]
	v_pk_fma_f32 v[4:5], v[18:19], v[4:5], v[18:19] op_sel_hi:[0,1,0]
	v_rcp_f32_e32 v8, v8
	v_rcp_f32_e32 v9, v9
	v_rcp_f32_e32 v4, v4
	v_rcp_f32_e32 v5, v5
	v_pk_mul_f32 v[6:7], v[14:15], v[6:7]
	v_pk_mul_f32 v[2:3], v[10:11], v[2:3]
	v_med3_f32 v6, v6, s49, v164
	v_med3_f32 v7, v7, s49, v164
	v_med3_f32 v2, v2, s49, v164
	v_med3_f32 v3, v3, s49, v164
	v_cvt_pk_fp8_f32 v20, v6, v7
	v_cvt_pk_fp8_f32 v21, v2, v3
	v_pk_mul_f32 v[8:9], v[16:17], v[8:9]
	v_pk_mul_f32 v[4:5], v[12:13], v[4:5]
	v_med3_f32 v8, v8, s49, v164
	v_med3_f32 v9, v9, s49, v164
	v_med3_f32 v2, v4, s49, v164
	v_med3_f32 v3, v5, s49, v164
	v_cvt_pk_fp8_f32 v20, v8, v9 op_sel:[0,0,1]
	v_cvt_pk_fp8_f32 v21, v2, v3 op_sel:[0,0,1]
	v_mad_i64_i32 v[2:3], s[26:27], v23, s48, v[150:151]
	v_lshl_add_u64 v[2:3], v[2:3], 0, v[148:149]
	global_store_dwordx2 v[2:3], v[20:21], off
	s_cbranch_vccnz .LBB0_467
	s_andn2_b64 vcc, exec, s[6:7]
	s_cbranch_vccnz .LBB0_466
	s_barrier
	s_branch .LBB0_466

.LBB0_654:
	v_lshl_add_u32 v152, s0, 8, v154
	v_ashrrev_i32_e32 v153, 31, v152
	v_lshl_add_u64 v[148:149], v[152:153], 3, s[12:13]
	global_load_dwordx2 v[150:151], v[148:149], off
	global_load_dwordx2 v[178:179], v[148:149], off offset:128
	global_load_dwordx2 v[180:181], v[148:149], off offset:256
	global_load_dwordx2 v[182:183], v[148:149], off offset:384
	global_load_dwordx2 v[184:185], v[148:149], off offset:1024
	global_load_dwordx2 v[186:187], v[148:149], off offset:1152
	global_load_dwordx2 v[188:189], v[148:149], off offset:1280
	global_load_dwordx2 v[190:191], v[148:149], off offset:1408
	v_lshlrev_b64 v[166:167], 14, v[152:153]
	v_lshl_or_b32 v162, s1, 8, v156
	v_ashrrev_i32_e32 v163, 31, v162
	v_or_b32_e32 v164, 16, v152
	v_lshlrev_b64 v[162:163], 1, v[162:163]
	v_ashrrev_i32_e32 v165, 31, v164
	s_mov_b64 s[0:1], 0x200000
	s_waitcnt vmcnt(7)
	v_ffbh_u32_e32 v153, v151
	v_min_u32_e32 v153, 32, v153
	v_lshlrev_b64 v[150:151], v153, v[150:151]
	v_min_u32_e32 v150, 1, v150
	v_or_b32_e32 v150, v151, v150
	v_cvt_f32_u32_e32 v150, v150
	v_sub_u32_e32 v151, 32, v153
	v_ldexp_f32 v150, v150, v151
	v_fmamk_f32 v150, v150, 0x30000000, v161
	v_rsq_f32_e32 v168, v150
	v_lshl_add_u64 v[150:151], s[10:11], 0, v[166:167]
	v_lshl_add_u64 v[150:151], v[150:151], 0, v[162:163]
	v_lshl_add_u64 v[166:167], v[164:165], 3, s[12:13]
	v_pk_mul_f32 v[128:129], v[128:129], v[168:169] op_sel_hi:[1,0]
	v_pk_mul_f32 v[126:127], v[126:127], v[168:169] op_sel_hi:[1,0]
	v_pk_mul_f32 v[124:125], v[124:125], v[168:169] op_sel_hi:[1,0]
	v_pk_mul_f32 v[122:123], v[122:123], v[168:169] op_sel_hi:[1,0]
	v_pk_mul_f32 v[120:121], v[120:121], v[168:169] op_sel_hi:[1,0]
	v_pk_mul_f32 v[118:119], v[118:119], v[168:169] op_sel_hi:[1,0]
	v_pk_mul_f32 v[170:171], v[116:117], v[168:169] op_sel_hi:[1,0]
	v_pk_mul_f32 v[168:169], v[114:115], v[168:169] op_sel_hi:[1,0]
	v_cvt_pk_bf16_f32 v114, v126, v127
	v_cvt_pk_bf16_f32 v115, v128, v129
	v_cvt_pk_bf16_f32 v116, v122, v123
	v_cvt_pk_bf16_f32 v117, v124, v125
	global_store_dwordx4 v[150:151], v[114:117], off
	s_nop 1
	v_cvt_pk_bf16_f32 v114, v118, v119
	v_cvt_pk_bf16_f32 v115, v120, v121
	v_cvt_pk_bf16_f32 v116, v168, v169
	v_cvt_pk_bf16_f32 v117, v170, v171
	global_store_dwordx4 v[150:151], v[114:117], off offset:256
	s_nop 0
	s_nop 0
	v_or_b32_e32 v116, 32, v152
	s_waitcnt vmcnt(8)
	v_mov_b32_e32 v114, v178
	v_mov_b32_e32 v115, v179
	v_ffbh_u32_e32 v117, v115
	v_min_u32_e32 v118, 32, v117
	v_lshlrev_b64 v[114:115], v118, v[114:115]
	v_min_u32_e32 v114, 1, v114
	v_or_b32_e32 v114, v115, v114
	v_cvt_f32_u32_e32 v119, v114
	v_sub_u32_e32 v118, 32, v118
	v_lshlrev_b64 v[114:115], 14, v[164:165]
	v_lshl_add_u64 v[114:115], s[10:11], 0, v[114:115]
	v_ldexp_f32 v118, v119, v118
	v_fmamk_f32 v118, v118, 0x30000000, v161
	v_rsq_f32_e32 v118, v118
	v_ashrrev_i32_e32 v117, 31, v116
	v_lshl_add_u64 v[114:115], v[114:115], 0, v[162:163]
	v_lshl_add_u64 v[120:121], v[116:117], 3, s[12:13]
	v_pk_mul_f32 v[112:113], v[112:113], v[118:119] op_sel_hi:[1,0]
	v_pk_mul_f32 v[110:111], v[110:111], v[118:119] op_sel_hi:[1,0]
	v_pk_mul_f32 v[108:109], v[108:109], v[118:119] op_sel_hi:[1,0]
	v_pk_mul_f32 v[106:107], v[106:107], v[118:119] op_sel_hi:[1,0]
	v_pk_mul_f32 v[104:105], v[104:105], v[118:119] op_sel_hi:[1,0]
	v_pk_mul_f32 v[102:103], v[102:103], v[118:119] op_sel_hi:[1,0]
	v_pk_mul_f32 v[122:123], v[100:101], v[118:119] op_sel_hi:[1,0]
	v_pk_mul_f32 v[118:119], v[98:99], v[118:119] op_sel_hi:[1,0]
	v_cvt_pk_bf16_f32 v98, v110, v111
	v_cvt_pk_bf16_f32 v99, v112, v113
	v_cvt_pk_bf16_f32 v100, v106, v107
	v_cvt_pk_bf16_f32 v101, v108, v109
	global_store_dwordx4 v[114:115], v[98:101], off
	s_nop 1
	v_cvt_pk_bf16_f32 v98, v102, v103
	v_cvt_pk_bf16_f32 v99, v104, v105
	v_cvt_pk_bf16_f32 v100, v118, v119
	v_cvt_pk_bf16_f32 v101, v122, v123
	global_store_dwordx4 v[114:115], v[98:101], off offset:256
	s_nop 0
	s_nop 0
	v_or_b32_e32 v100, 48, v152
	s_waitcnt vmcnt(9)
	v_mov_b32_e32 v98, v180
	v_mov_b32_e32 v99, v181
	v_ffbh_u32_e32 v101, v99
	v_min_u32_e32 v102, 32, v101
	v_lshlrev_b64 v[98:99], v102, v[98:99]
	v_min_u32_e32 v98, 1, v98
	v_or_b32_e32 v98, v99, v98
	v_cvt_f32_u32_e32 v103, v98
	v_sub_u32_e32 v102, 32, v102
	v_lshlrev_b64 v[98:99], 14, v[116:117]
	v_lshl_add_u64 v[98:99], s[10:11], 0, v[98:99]
	v_ldexp_f32 v102, v103, v102
	v_fmamk_f32 v102, v102, 0x30000000, v161
	v_rsq_f32_e32 v102, v102
	v_ashrrev_i32_e32 v101, 31, v100
	v_lshl_add_u64 v[98:99], v[98:99], 0, v[162:163]
	v_lshl_add_u64 v[104:105], v[100:101], 3, s[12:13]
	v_pk_mul_f32 v[96:97], v[96:97], v[102:103] op_sel_hi:[1,0]
	v_pk_mul_f32 v[94:95], v[94:95], v[102:103] op_sel_hi:[1,0]
	v_pk_mul_f32 v[92:93], v[92:93], v[102:103] op_sel_hi:[1,0]
	v_pk_mul_f32 v[90:91], v[90:91], v[102:103] op_sel_hi:[1,0]
	v_pk_mul_f32 v[88:89], v[88:89], v[102:103] op_sel_hi:[1,0]
	v_pk_mul_f32 v[86:87], v[86:87], v[102:103] op_sel_hi:[1,0]
	v_pk_mul_f32 v[106:107], v[84:85], v[102:103] op_sel_hi:[1,0]
	v_pk_mul_f32 v[102:103], v[82:83], v[102:103] op_sel_hi:[1,0]
	v_cvt_pk_bf16_f32 v82, v94, v95
	v_cvt_pk_bf16_f32 v83, v96, v97
	v_cvt_pk_bf16_f32 v84, v90, v91
	v_cvt_pk_bf16_f32 v85, v92, v93
	global_store_dwordx4 v[98:99], v[82:85], off
	s_nop 1
	v_cvt_pk_bf16_f32 v82, v86, v87
	v_cvt_pk_bf16_f32 v83, v88, v89
	v_cvt_pk_bf16_f32 v84, v102, v103
	v_cvt_pk_bf16_f32 v85, v106, v107
	global_store_dwordx4 v[98:99], v[82:85], off offset:256
	s_nop 0
	s_waitcnt vmcnt(10)
	v_mov_b32_e32 v82, v182
	v_mov_b32_e32 v83, v183
	v_ffbh_u32_e32 v84, v83
	v_min_u32_e32 v84, 32, v84
	v_lshlrev_b64 v[82:83], v84, v[82:83]
	v_min_u32_e32 v82, 1, v82
	v_or_b32_e32 v82, v83, v82
	v_cvt_f32_u32_e32 v82, v82
	v_sub_u32_e32 v83, 32, v84
	v_lshlrev_b64 v[84:85], 14, v[100:101]
	v_lshl_add_u64 v[84:85], s[10:11], 0, v[84:85]
	v_ldexp_f32 v82, v82, v83
	v_fmamk_f32 v82, v82, 0x30000000, v161
	v_rsq_f32_e32 v82, v82
	v_lshl_add_u64 v[84:85], v[84:85], 0, v[162:163]
	v_pk_mul_f32 v[80:81], v[80:81], v[82:83] op_sel_hi:[1,0]
	v_pk_mul_f32 v[78:79], v[78:79], v[82:83] op_sel_hi:[1,0]
	v_pk_mul_f32 v[76:77], v[76:77], v[82:83] op_sel_hi:[1,0]
	v_pk_mul_f32 v[74:75], v[74:75], v[82:83] op_sel_hi:[1,0]
	v_pk_mul_f32 v[72:73], v[72:73], v[82:83] op_sel_hi:[1,0]
	v_pk_mul_f32 v[70:71], v[70:71], v[82:83] op_sel_hi:[1,0]
	v_pk_mul_f32 v[86:87], v[68:69], v[82:83] op_sel_hi:[1,0]
	v_pk_mul_f32 v[82:83], v[66:67], v[82:83] op_sel_hi:[1,0]
	v_cvt_pk_bf16_f32 v66, v78, v79
	v_cvt_pk_bf16_f32 v67, v80, v81
	v_cvt_pk_bf16_f32 v68, v74, v75
	v_cvt_pk_bf16_f32 v69, v76, v77
	global_store_dwordx4 v[84:85], v[66:69], off
	s_nop 1
	v_cvt_pk_bf16_f32 v66, v70, v71
	v_cvt_pk_bf16_f32 v67, v72, v73
	v_cvt_pk_bf16_f32 v68, v82, v83
	v_cvt_pk_bf16_f32 v69, v86, v87
	global_store_dwordx4 v[84:85], v[66:69], off offset:256
	s_nop 0
	v_add_co_u32_e32 v70, vcc, s58, v150
	s_waitcnt vmcnt(11)
	v_mov_b32_e32 v66, v184
	v_mov_b32_e32 v67, v185
	v_ffbh_u32_e32 v68, v67
	v_min_u32_e32 v68, 32, v68
	v_lshlrev_b64 v[66:67], v68, v[66:67]
	v_min_u32_e32 v66, 1, v66
	v_or_b32_e32 v66, v67, v66
	v_cvt_f32_u32_e32 v69, v66
	v_sub_u32_e32 v68, 32, v68
	v_lshl_add_u64 v[66:67], v[150:151], 0, s[0:1]
	v_addc_co_u32_e32 v71, vcc, 0, v151, vcc
	v_ldexp_f32 v68, v69, v68
	v_fmamk_f32 v68, v68, 0x30000000, v161
	v_rsq_f32_e32 v68, v68
	s_nop 0
	v_pk_mul_f32 v[64:65], v[64:65], v[68:69] op_sel_hi:[1,0]
	v_pk_mul_f32 v[62:63], v[62:63], v[68:69] op_sel_hi:[1,0]
	v_pk_mul_f32 v[60:61], v[60:61], v[68:69] op_sel_hi:[1,0]
	v_pk_mul_f32 v[58:59], v[58:59], v[68:69] op_sel_hi:[1,0]
	v_pk_mul_f32 v[56:57], v[56:57], v[68:69] op_sel_hi:[1,0]
	v_pk_mul_f32 v[54:55], v[54:55], v[68:69] op_sel_hi:[1,0]
	v_pk_mul_f32 v[72:73], v[52:53], v[68:69] op_sel_hi:[1,0]
	v_pk_mul_f32 v[68:69], v[50:51], v[68:69] op_sel_hi:[1,0]
	v_cvt_pk_bf16_f32 v50, v62, v63
	v_cvt_pk_bf16_f32 v51, v64, v65
	v_cvt_pk_bf16_f32 v52, v58, v59
	v_cvt_pk_bf16_f32 v53, v60, v61
	global_store_dwordx4 v[70:71], v[50:53], off
	s_nop 1
	v_cvt_pk_bf16_f32 v50, v54, v55
	v_cvt_pk_bf16_f32 v51, v56, v57
	v_cvt_pk_bf16_f32 v52, v68, v69
	v_cvt_pk_bf16_f32 v53, v72, v73
	global_store_dwordx4 v[66:67], v[50:53], off offset:256
	s_nop 0
	v_add_co_u32_e32 v54, vcc, s59, v150
	s_waitcnt vmcnt(12)
	v_mov_b32_e32 v50, v186
	v_mov_b32_e32 v51, v187
	v_ffbh_u32_e32 v52, v51
	v_min_u32_e32 v52, 32, v52
	v_lshlrev_b64 v[50:51], v52, v[50:51]
	v_min_u32_e32 v50, 1, v50
	v_or_b32_e32 v50, v51, v50
	v_cvt_f32_u32_e32 v53, v50
	v_sub_u32_e32 v52, 32, v52
	v_lshl_add_u64 v[50:51], v[150:151], 0, s[18:19]
	v_addc_co_u32_e32 v55, vcc, 0, v151, vcc
	v_ldexp_f32 v52, v53, v52
	v_fmamk_f32 v52, v52, 0x30000000, v161
	v_rsq_f32_e32 v52, v52
	s_nop 0
	v_pk_mul_f32 v[48:49], v[48:49], v[52:53] op_sel_hi:[1,0]
	v_pk_mul_f32 v[46:47], v[46:47], v[52:53] op_sel_hi:[1,0]
	v_pk_mul_f32 v[44:45], v[44:45], v[52:53] op_sel_hi:[1,0]
	v_pk_mul_f32 v[42:43], v[42:43], v[52:53] op_sel_hi:[1,0]
	v_pk_mul_f32 v[40:41], v[40:41], v[52:53] op_sel_hi:[1,0]
	v_pk_mul_f32 v[38:39], v[38:39], v[52:53] op_sel_hi:[1,0]
	v_pk_mul_f32 v[56:57], v[36:37], v[52:53] op_sel_hi:[1,0]
	v_pk_mul_f32 v[52:53], v[34:35], v[52:53] op_sel_hi:[1,0]
	v_cvt_pk_bf16_f32 v34, v46, v47
	v_cvt_pk_bf16_f32 v35, v48, v49
	v_cvt_pk_bf16_f32 v36, v42, v43
	v_cvt_pk_bf16_f32 v37, v44, v45
	global_store_dwordx4 v[54:55], v[34:37], off
	s_nop 1
	v_cvt_pk_bf16_f32 v34, v38, v39
	v_cvt_pk_bf16_f32 v35, v40, v41
	v_cvt_pk_bf16_f32 v36, v52, v53
	v_cvt_pk_bf16_f32 v37, v56, v57
	global_store_dwordx4 v[50:51], v[34:37], off offset:256
	s_nop 0
	v_add_co_u32_e32 v38, vcc, s60, v150
	s_waitcnt vmcnt(13)
	v_mov_b32_e32 v34, v188
	v_mov_b32_e32 v35, v189
	v_ffbh_u32_e32 v36, v35
	v_min_u32_e32 v36, 32, v36
	v_lshlrev_b64 v[34:35], v36, v[34:35]
	v_min_u32_e32 v34, 1, v34
	v_or_b32_e32 v34, v35, v34
	v_cvt_f32_u32_e32 v37, v34
	v_sub_u32_e32 v36, 32, v36
	v_lshl_add_u64 v[34:35], v[150:151], 0, s[20:21]
	v_addc_co_u32_e32 v39, vcc, 0, v151, vcc
	v_ldexp_f32 v36, v37, v36
	v_fmamk_f32 v36, v36, 0x30000000, v161
	v_rsq_f32_e32 v36, v36
	s_andn2_b64 vcc, exec, s[4:5]
	v_pk_mul_f32 v[32:33], v[32:33], v[36:37] op_sel_hi:[1,0]
	v_pk_mul_f32 v[30:31], v[30:31], v[36:37] op_sel_hi:[1,0]
	v_pk_mul_f32 v[28:29], v[28:29], v[36:37] op_sel_hi:[1,0]
	v_pk_mul_f32 v[26:27], v[26:27], v[36:37] op_sel_hi:[1,0]
	v_pk_mul_f32 v[24:25], v[24:25], v[36:37] op_sel_hi:[1,0]
	v_pk_mul_f32 v[22:23], v[22:23], v[36:37] op_sel_hi:[1,0]
	v_pk_mul_f32 v[40:41], v[20:21], v[36:37] op_sel_hi:[1,0]
	v_pk_mul_f32 v[36:37], v[18:19], v[36:37] op_sel_hi:[1,0]
	v_cvt_pk_bf16_f32 v18, v30, v31
	v_cvt_pk_bf16_f32 v19, v32, v33
	v_cvt_pk_bf16_f32 v20, v26, v27
	v_cvt_pk_bf16_f32 v21, v28, v29
	global_store_dwordx4 v[38:39], v[18:21], off
	s_nop 1
	v_cvt_pk_bf16_f32 v18, v22, v23
	v_cvt_pk_bf16_f32 v19, v24, v25
	v_cvt_pk_bf16_f32 v20, v36, v37
	v_cvt_pk_bf16_f32 v21, v40, v41
	global_store_dwordx4 v[34:35], v[18:21], off offset:256
	s_nop 0
	v_add_co_u32_e64 v22, s[0:1], s61, v150
	s_waitcnt vmcnt(14)
	v_mov_b32_e32 v18, v190
	v_mov_b32_e32 v19, v191
	v_ffbh_u32_e32 v20, v19
	v_min_u32_e32 v20, 32, v20
	v_lshlrev_b64 v[18:19], v20, v[18:19]
	v_min_u32_e32 v18, 1, v18
	v_or_b32_e32 v18, v19, v18
	v_cvt_f32_u32_e32 v21, v18
	v_sub_u32_e32 v20, 32, v20
	v_addc_co_u32_e64 v23, s[0:1], 0, v151, s[0:1]
	v_ldexp_f32 v20, v21, v20
	v_fmamk_f32 v20, v20, 0x30000000, v161
	v_rsq_f32_e32 v20, v20
	v_lshl_add_u64 v[18:19], v[150:151], 0, s[22:23]
	s_mov_b64 s[0:1], -1
	v_pk_mul_f32 v[16:17], v[16:17], v[20:21] op_sel_hi:[1,0]
	v_pk_mul_f32 v[14:15], v[14:15], v[20:21] op_sel_hi:[1,0]
	v_pk_mul_f32 v[12:13], v[12:13], v[20:21] op_sel_hi:[1,0]
	v_pk_mul_f32 v[10:11], v[10:11], v[20:21] op_sel_hi:[1,0]
	v_pk_mul_f32 v[8:9], v[8:9], v[20:21] op_sel_hi:[1,0]
	v_pk_mul_f32 v[6:7], v[6:7], v[20:21] op_sel_hi:[1,0]
	v_pk_mul_f32 v[24:25], v[4:5], v[20:21] op_sel_hi:[1,0]
	v_pk_mul_f32 v[20:21], v[2:3], v[20:21] op_sel_hi:[1,0]
	v_cvt_pk_bf16_f32 v2, v14, v15
	v_cvt_pk_bf16_f32 v3, v16, v17
	v_cvt_pk_bf16_f32 v4, v10, v11
	v_cvt_pk_bf16_f32 v5, v12, v13
	global_store_dwordx4 v[22:23], v[2:5], off
	s_nop 1
	v_cvt_pk_bf16_f32 v2, v6, v7
	v_cvt_pk_bf16_f32 v3, v8, v9
	v_cvt_pk_bf16_f32 v4, v20, v21
	v_cvt_pk_bf16_f32 v5, v24, v25
	global_store_dwordx4 v[18:19], v[2:5], off offset:256
	s_cbranch_vccnz .LBB0_643
	s_andn2_b64 vcc, exec, s[8:9]
	s_cbranch_vccnz .LBB0_642
	s_barrier
	s_branch .LBB0_642

.LBB0_1162:
	v_lshl_add_u32 v166, s0, 8, v157
	v_ashrrev_i32_e32 v167, 31, v166
	v_lshl_add_u64 v[144:145], v[166:167], 2, s[6:7]
	global_load_dword v168, v[144:145], off
	global_load_dword v178, v[144:145], off offset:64
	global_load_dword v179, v[144:145], off offset:128
	global_load_dword v180, v[144:145], off offset:192
	global_load_dword v181, v[144:145], off offset:512
	global_load_dword v182, v[144:145], off offset:576
	global_load_dword v183, v[144:145], off offset:640
	global_load_dword v184, v[144:145], off offset:704
	v_lshl_or_b32 v148, s67, 8, v159
	v_ashrrev_i32_e32 v149, 31, v148
	v_lshlrev_b64 v[172:173], 12, v[166:167]
	v_or_b32_e32 v170, 16, v166
	v_lshlrev_b64 v[174:175], 1, v[148:149]
	v_lshl_add_u64 v[148:149], s[12:13], 0, v[172:173]
	v_ashrrev_i32_e32 v171, 31, v170
	v_lshl_add_u64 v[148:149], v[148:149], 0, v[174:175]
	v_lshl_add_u64 v[172:173], v[170:171], 2, s[6:7]
	s_waitcnt vmcnt(7)
	v_pk_mul_f32 v[128:129], v[128:129], v[168:169] op_sel_hi:[1,0]
	v_pk_mul_f32 v[126:127], v[126:127], v[168:169] op_sel_hi:[1,0]
	v_pk_mul_f32 v[124:125], v[124:125], v[168:169] op_sel_hi:[1,0]
	v_pk_mul_f32 v[122:123], v[122:123], v[168:169] op_sel_hi:[1,0]
	v_pk_mul_f32 v[120:121], v[120:121], v[168:169] op_sel_hi:[1,0]
	v_pk_mul_f32 v[118:119], v[118:119], v[168:169] op_sel_hi:[1,0]
	v_pk_mul_f32 v[176:177], v[116:117], v[168:169] op_sel_hi:[1,0]
	v_pk_mul_f32 v[168:169], v[114:115], v[168:169] op_sel_hi:[1,0]
	v_cvt_pk_bf16_f32 v114, v126, v127
	v_cvt_pk_bf16_f32 v115, v128, v129
	v_cvt_pk_bf16_f32 v116, v122, v123
	v_cvt_pk_bf16_f32 v117, v124, v125
	global_store_dwordx4 v[148:149], v[114:117], off
	s_nop 1
	v_cvt_pk_bf16_f32 v114, v118, v119
	v_cvt_pk_bf16_f32 v115, v120, v121
	v_cvt_pk_bf16_f32 v116, v168, v169
	v_cvt_pk_bf16_f32 v117, v176, v177
	global_store_dwordx4 v[148:149], v[114:117], off offset:256
	s_nop 0
	v_lshlrev_b64 v[118:119], 12, v[170:171]
	v_or_b32_e32 v116, 32, v166
	v_lshl_add_u64 v[118:119], s[12:13], 0, v[118:119]
	v_ashrrev_i32_e32 v117, 31, v116
	v_lshl_add_u64 v[118:119], v[118:119], 0, v[174:175]
	v_lshl_add_u64 v[120:121], v[116:117], 2, s[6:7]
	s_waitcnt vmcnt(8)
	v_mov_b32_e32 v114, v178
	v_pk_mul_f32 v[112:113], v[112:113], v[114:115] op_sel_hi:[1,0]
	v_pk_mul_f32 v[110:111], v[110:111], v[114:115] op_sel_hi:[1,0]
	v_pk_mul_f32 v[108:109], v[108:109], v[114:115] op_sel_hi:[1,0]
	v_pk_mul_f32 v[106:107], v[106:107], v[114:115] op_sel_hi:[1,0]
	v_pk_mul_f32 v[104:105], v[104:105], v[114:115] op_sel_hi:[1,0]
	v_pk_mul_f32 v[102:103], v[102:103], v[114:115] op_sel_hi:[1,0]
	v_pk_mul_f32 v[122:123], v[100:101], v[114:115] op_sel_hi:[1,0]
	v_pk_mul_f32 v[114:115], v[98:99], v[114:115] op_sel_hi:[1,0]
	v_cvt_pk_bf16_f32 v98, v110, v111
	v_cvt_pk_bf16_f32 v99, v112, v113
	v_cvt_pk_bf16_f32 v100, v106, v107
	v_cvt_pk_bf16_f32 v101, v108, v109
	global_store_dwordx4 v[118:119], v[98:101], off
	s_nop 1
	v_cvt_pk_bf16_f32 v98, v102, v103
	v_cvt_pk_bf16_f32 v99, v104, v105
	v_cvt_pk_bf16_f32 v100, v114, v115
	v_cvt_pk_bf16_f32 v101, v122, v123
	global_store_dwordx4 v[118:119], v[98:101], off offset:256
	s_nop 0
	v_lshlrev_b64 v[102:103], 12, v[116:117]
	v_or_b32_e32 v100, 48, v166
	v_lshl_add_u64 v[102:103], s[12:13], 0, v[102:103]
	v_ashrrev_i32_e32 v101, 31, v100
	v_lshl_add_u64 v[102:103], v[102:103], 0, v[174:175]
	v_lshl_add_u64 v[104:105], v[100:101], 2, s[6:7]
	s_waitcnt vmcnt(9)
	v_mov_b32_e32 v98, v179
	v_pk_mul_f32 v[96:97], v[96:97], v[98:99] op_sel_hi:[1,0]
	v_pk_mul_f32 v[94:95], v[94:95], v[98:99] op_sel_hi:[1,0]
	v_pk_mul_f32 v[92:93], v[92:93], v[98:99] op_sel_hi:[1,0]
	v_pk_mul_f32 v[90:91], v[90:91], v[98:99] op_sel_hi:[1,0]
	v_pk_mul_f32 v[84:85], v[84:85], v[98:99] op_sel_hi:[1,0]
	v_pk_mul_f32 v[82:83], v[82:83], v[98:99] op_sel_hi:[1,0]
	v_pk_mul_f32 v[106:107], v[76:77], v[98:99] op_sel_hi:[1,0]
	v_pk_mul_f32 v[98:99], v[74:75], v[98:99] op_sel_hi:[1,0]
	v_cvt_pk_bf16_f32 v74, v94, v95
	v_cvt_pk_bf16_f32 v75, v96, v97
	v_cvt_pk_bf16_f32 v76, v90, v91
	v_cvt_pk_bf16_f32 v77, v92, v93
	global_store_dwordx4 v[102:103], v[74:77], off
	s_nop 1
	v_cvt_pk_bf16_f32 v74, v82, v83
	v_cvt_pk_bf16_f32 v75, v84, v85
	v_cvt_pk_bf16_f32 v76, v98, v99
	v_cvt_pk_bf16_f32 v77, v106, v107
	global_store_dwordx4 v[102:103], v[74:77], off offset:256
	s_nop 0
	s_waitcnt vmcnt(10)
	v_mov_b32_e32 v74, v180
	v_pk_mul_f32 v[82:83], v[88:89], v[74:75] op_sel_hi:[1,0]
	v_lshlrev_b64 v[76:77], 12, v[100:101]
	v_lshl_add_u64 v[76:77], s[12:13], 0, v[76:77]
	v_lshl_add_u64 v[76:77], v[76:77], 0, v[174:175]
	v_pk_mul_f32 v[84:85], v[86:87], v[74:75] op_sel_hi:[1,0]
	v_pk_mul_f32 v[80:81], v[80:81], v[74:75] op_sel_hi:[1,0]
	v_pk_mul_f32 v[78:79], v[78:79], v[74:75] op_sel_hi:[1,0]
	v_pk_mul_f32 v[72:73], v[72:73], v[74:75] op_sel_hi:[1,0]
	v_pk_mul_f32 v[70:71], v[70:71], v[74:75] op_sel_hi:[1,0]
	v_pk_mul_f32 v[86:87], v[68:69], v[74:75] op_sel_hi:[1,0]
	v_pk_mul_f32 v[74:75], v[66:67], v[74:75] op_sel_hi:[1,0]
	v_cvt_pk_bf16_f32 v66, v84, v85
	v_cvt_pk_bf16_f32 v67, v82, v83
	v_cvt_pk_bf16_f32 v68, v78, v79
	v_cvt_pk_bf16_f32 v69, v80, v81
	global_store_dwordx4 v[76:77], v[66:69], off
	s_nop 1
	v_cvt_pk_bf16_f32 v66, v70, v71
	v_cvt_pk_bf16_f32 v67, v72, v73
	v_cvt_pk_bf16_f32 v68, v74, v75
	v_cvt_pk_bf16_f32 v69, v86, v87
	global_store_dwordx4 v[76:77], v[66:69], off offset:256
	s_nop 0
	v_add_co_u32_e32 v70, vcc, s60, v148
	v_lshl_add_u64 v[68:69], v[148:149], 0, s[18:19]
	s_nop 0
	v_addc_co_u32_e32 v71, vcc, 0, v149, vcc
	s_waitcnt vmcnt(11)
	v_mov_b32_e32 v66, v181
	v_pk_mul_f32 v[64:65], v[64:65], v[66:67] op_sel_hi:[1,0]
	v_pk_mul_f32 v[62:63], v[62:63], v[66:67] op_sel_hi:[1,0]
	v_pk_mul_f32 v[60:61], v[60:61], v[66:67] op_sel_hi:[1,0]
	v_pk_mul_f32 v[58:59], v[58:59], v[66:67] op_sel_hi:[1,0]
	v_pk_mul_f32 v[56:57], v[56:57], v[66:67] op_sel_hi:[1,0]
	v_pk_mul_f32 v[54:55], v[54:55], v[66:67] op_sel_hi:[1,0]
	v_pk_mul_f32 v[72:73], v[52:53], v[66:67] op_sel_hi:[1,0]
	v_pk_mul_f32 v[66:67], v[50:51], v[66:67] op_sel_hi:[1,0]
	v_cvt_pk_bf16_f32 v50, v62, v63
	v_cvt_pk_bf16_f32 v51, v64, v65
	v_cvt_pk_bf16_f32 v52, v58, v59
	v_cvt_pk_bf16_f32 v53, v60, v61
	global_store_dwordx4 v[70:71], v[50:53], off
	s_nop 1
	v_cvt_pk_bf16_f32 v50, v54, v55
	v_cvt_pk_bf16_f32 v51, v56, v57
	v_cvt_pk_bf16_f32 v52, v66, v67
	v_cvt_pk_bf16_f32 v53, v72, v73
	global_store_dwordx4 v[68:69], v[50:53], off offset:256
	s_nop 0
	v_add_co_u32_e32 v54, vcc, s61, v148
	v_lshl_add_u64 v[52:53], v[148:149], 0, s[20:21]
	s_nop 0
	v_addc_co_u32_e32 v55, vcc, 0, v149, vcc
	s_waitcnt vmcnt(12)
	v_mov_b32_e32 v50, v182
	v_pk_mul_f32 v[48:49], v[48:49], v[50:51] op_sel_hi:[1,0]
	v_pk_mul_f32 v[46:47], v[46:47], v[50:51] op_sel_hi:[1,0]
	v_pk_mul_f32 v[44:45], v[44:45], v[50:51] op_sel_hi:[1,0]
	v_pk_mul_f32 v[42:43], v[42:43], v[50:51] op_sel_hi:[1,0]
	v_pk_mul_f32 v[40:41], v[40:41], v[50:51] op_sel_hi:[1,0]
	v_pk_mul_f32 v[38:39], v[38:39], v[50:51] op_sel_hi:[1,0]
	v_pk_mul_f32 v[56:57], v[36:37], v[50:51] op_sel_hi:[1,0]
	v_pk_mul_f32 v[50:51], v[34:35], v[50:51] op_sel_hi:[1,0]
	v_cvt_pk_bf16_f32 v34, v46, v47
	v_cvt_pk_bf16_f32 v35, v48, v49
	v_cvt_pk_bf16_f32 v36, v42, v43
	v_cvt_pk_bf16_f32 v37, v44, v45
	global_store_dwordx4 v[54:55], v[34:37], off
	s_nop 1
	v_cvt_pk_bf16_f32 v34, v38, v39
	v_cvt_pk_bf16_f32 v35, v40, v41
	v_cvt_pk_bf16_f32 v36, v50, v51
	v_cvt_pk_bf16_f32 v37, v56, v57
	global_store_dwordx4 v[52:53], v[34:37], off offset:256
	s_nop 0
	v_add_co_u32_e32 v38, vcc, s62, v148
	v_lshl_add_u64 v[36:37], v[148:149], 0, s[22:23]
	s_nop 0
	v_addc_co_u32_e32 v39, vcc, 0, v149, vcc
	s_and_b64 vcc, exec, s[2:3]
	s_waitcnt vmcnt(13)
	v_mov_b32_e32 v34, v183
	v_pk_mul_f32 v[32:33], v[32:33], v[34:35] op_sel_hi:[1,0]
	v_pk_mul_f32 v[30:31], v[30:31], v[34:35] op_sel_hi:[1,0]
	v_pk_mul_f32 v[28:29], v[28:29], v[34:35] op_sel_hi:[1,0]
	v_pk_mul_f32 v[26:27], v[26:27], v[34:35] op_sel_hi:[1,0]
	v_pk_mul_f32 v[24:25], v[24:25], v[34:35] op_sel_hi:[1,0]
	v_pk_mul_f32 v[22:23], v[22:23], v[34:35] op_sel_hi:[1,0]
	v_pk_mul_f32 v[40:41], v[20:21], v[34:35] op_sel_hi:[1,0]
	v_pk_mul_f32 v[34:35], v[18:19], v[34:35] op_sel_hi:[1,0]
	v_cvt_pk_bf16_f32 v18, v30, v31
	v_cvt_pk_bf16_f32 v19, v32, v33
	v_cvt_pk_bf16_f32 v20, v26, v27
	v_cvt_pk_bf16_f32 v21, v28, v29
	global_store_dwordx4 v[38:39], v[18:21], off
	s_nop 1
	v_cvt_pk_bf16_f32 v18, v22, v23
	v_cvt_pk_bf16_f32 v19, v24, v25
	v_cvt_pk_bf16_f32 v20, v34, v35
	v_cvt_pk_bf16_f32 v21, v40, v41
	global_store_dwordx4 v[36:37], v[18:21], off offset:256
	s_nop 0
	v_add_co_u32_e64 v22, s[0:1], s63, v148
	v_lshl_add_u64 v[20:21], v[148:149], 0, s[24:25]
	s_nop 0
	v_addc_co_u32_e64 v23, s[0:1], 0, v149, s[0:1]
	s_mov_b64 s[0:1], -1
	s_waitcnt vmcnt(14)
	v_mov_b32_e32 v18, v184
	v_pk_mul_f32 v[16:17], v[16:17], v[18:19] op_sel_hi:[1,0]
	v_pk_mul_f32 v[14:15], v[14:15], v[18:19] op_sel_hi:[1,0]
	v_pk_mul_f32 v[12:13], v[12:13], v[18:19] op_sel_hi:[1,0]
	v_pk_mul_f32 v[10:11], v[10:11], v[18:19] op_sel_hi:[1,0]
	v_pk_mul_f32 v[8:9], v[8:9], v[18:19] op_sel_hi:[1,0]
	v_pk_mul_f32 v[6:7], v[6:7], v[18:19] op_sel_hi:[1,0]
	v_pk_mul_f32 v[24:25], v[4:5], v[18:19] op_sel_hi:[1,0]
	v_pk_mul_f32 v[18:19], v[2:3], v[18:19] op_sel_hi:[1,0]
	v_cvt_pk_bf16_f32 v2, v14, v15
	v_cvt_pk_bf16_f32 v3, v16, v17
	v_cvt_pk_bf16_f32 v4, v10, v11
	v_cvt_pk_bf16_f32 v5, v12, v13
	global_store_dwordx4 v[22:23], v[2:5], off
	s_nop 1
	v_cvt_pk_bf16_f32 v2, v6, v7
	v_cvt_pk_bf16_f32 v3, v8, v9
	v_cvt_pk_bf16_f32 v4, v18, v19
	v_cvt_pk_bf16_f32 v5, v24, v25
	global_store_dwordx4 v[20:21], v[2:5], off offset:256
	s_cbranch_vccnz .LBB0_1151
	s_andn2_b64 vcc, exec, s[10:11]
	s_cbranch_vccnz .LBB0_1150
	s_barrier
	s_branch .LBB0_1150

.LBB0_1183:
	v_lshl_add_u32 v148, s20, 8, v147
	v_ashrrev_i32_e32 v149, 31, v148
	v_lshl_add_u64 v[140:141], v[148:149], 2, s[6:7]
	global_load_dword v158, v[140:141], off
	global_load_dword v178, v[140:141], off offset:64
	global_load_dword v179, v[140:141], off offset:128
	global_load_dword v180, v[140:141], off offset:192
	global_load_dword v181, v[140:141], off offset:512
	global_load_dword v182, v[140:141], off offset:576
	global_load_dword v183, v[140:141], off offset:640
	global_load_dword v184, v[140:141], off offset:704
	s_abs_i32 s22, s67
	s_mul_hi_u32 s23, s22, s61
	s_mul_i32 s24, s23, s59
	s_ashr_i32 s20, s67, 31
	s_sub_i32 s22, s22, s24
	s_xor_b32 s20, s20, s60
	s_add_i32 s25, s23, 1
	s_sub_i32 s24, s22, s59
	s_cmp_ge_u32 s22, s59
	s_cselect_b32 s23, s25, s23
	s_cselect_b32 s22, s24, s22
	s_add_i32 s24, s23, 1
	s_cmp_ge_u32 s22, s59
	s_cselect_b32 s22, s24, s23
	s_xor_b32 s22, s22, s20
	s_sub_i32 s20, s22, s20
	s_mul_hi_i32 s23, s53, s20
	s_mul_i32 s22, s53, s20
	s_lshl_b64 s[22:23], s[22:23], 1
	v_lshl_or_b32 v144, s66, 8, v151
	v_subrev_u32_e32 v142, s52, v148
	s_add_u32 s22, s50, s22
	v_ashrrev_i32_e32 v145, 31, v144
	v_ashrrev_i32_e32 v143, 31, v142
	s_addc_u32 s23, s51, s23
	v_or_b32_e32 v160, 16, v148
	v_lshlrev_b64 v[162:163], 12, v[142:143]
	v_lshl_add_u64 v[144:145], v[144:145], 1, s[22:23]
	v_ashrrev_i32_e32 v161, 31, v160
	v_lshl_add_u64 v[162:163], v[144:145], 0, v[162:163]
	v_lshl_add_u64 v[164:165], v[160:161], 2, s[6:7]
	s_and_b64 vcc, exec, s[2:3]
	s_mov_b64 s[2:3], -1
	s_waitcnt vmcnt(7)
	v_pk_mul_f32 v[122:123], v[122:123], v[158:159] op_sel_hi:[1,0]
	v_pk_mul_f32 v[120:121], v[120:121], v[158:159] op_sel_hi:[1,0]
	v_pk_mul_f32 v[126:127], v[126:127], v[158:159] op_sel_hi:[1,0]
	v_pk_mul_f32 v[124:125], v[124:125], v[158:159] op_sel_hi:[1,0]
	v_pk_mul_f32 v[118:119], v[118:119], v[158:159] op_sel_hi:[1,0]
	v_pk_mul_f32 v[116:117], v[116:117], v[158:159] op_sel_hi:[1,0]
	v_pk_mul_f32 v[166:167], v[114:115], v[158:159] op_sel_hi:[1,0]
	v_pk_mul_f32 v[158:159], v[112:113], v[158:159] op_sel_hi:[1,0]
	v_cvt_pk_bf16_f32 v112, v120, v121
	v_cvt_pk_bf16_f32 v113, v122, v123
	v_cvt_pk_bf16_f32 v114, v124, v125
	v_cvt_pk_bf16_f32 v115, v126, v127
	global_store_dwordx4 v[162:163], v[112:115], off
	s_nop 1
	v_cvt_pk_bf16_f32 v112, v116, v117
	v_cvt_pk_bf16_f32 v113, v118, v119
	v_cvt_pk_bf16_f32 v114, v158, v159
	v_cvt_pk_bf16_f32 v115, v166, v167
	global_store_dwordx4 v[162:163], v[112:115], off offset:256
	s_nop 0
	v_subrev_u32_e32 v116, s52, v160
	v_ashrrev_i32_e32 v117, 31, v116
	v_or_b32_e32 v114, 32, v148
	v_lshlrev_b64 v[116:117], 12, v[116:117]
	v_ashrrev_i32_e32 v115, 31, v114
	v_lshl_add_u64 v[116:117], v[144:145], 0, v[116:117]
	v_lshl_add_u64 v[118:119], v[114:115], 2, s[6:7]
	s_waitcnt vmcnt(8)
	v_mov_b32_e32 v112, v178
	v_pk_mul_f32 v[110:111], v[110:111], v[112:113] op_sel_hi:[1,0]
	v_pk_mul_f32 v[108:109], v[108:109], v[112:113] op_sel_hi:[1,0]
	v_pk_mul_f32 v[106:107], v[106:107], v[112:113] op_sel_hi:[1,0]
	v_pk_mul_f32 v[104:105], v[104:105], v[112:113] op_sel_hi:[1,0]
	v_pk_mul_f32 v[102:103], v[102:103], v[112:113] op_sel_hi:[1,0]
	v_pk_mul_f32 v[100:101], v[100:101], v[112:113] op_sel_hi:[1,0]
	v_pk_mul_f32 v[120:121], v[98:99], v[112:113] op_sel_hi:[1,0]
	v_pk_mul_f32 v[112:113], v[96:97], v[112:113] op_sel_hi:[1,0]
	v_cvt_pk_bf16_f32 v96, v108, v109
	v_cvt_pk_bf16_f32 v97, v110, v111
	v_cvt_pk_bf16_f32 v98, v104, v105
	v_cvt_pk_bf16_f32 v99, v106, v107
	global_store_dwordx4 v[116:117], v[96:99], off
	s_nop 1
	v_cvt_pk_bf16_f32 v96, v100, v101
	v_cvt_pk_bf16_f32 v97, v102, v103
	v_cvt_pk_bf16_f32 v98, v112, v113
	v_cvt_pk_bf16_f32 v99, v120, v121
	global_store_dwordx4 v[116:117], v[96:99], off offset:256
	s_nop 0
	v_subrev_u32_e32 v100, s52, v114
	v_ashrrev_i32_e32 v101, 31, v100
	v_or_b32_e32 v98, 48, v148
	v_lshlrev_b64 v[100:101], 12, v[100:101]
	v_ashrrev_i32_e32 v99, 31, v98
	v_lshl_add_u64 v[100:101], v[144:145], 0, v[100:101]
	v_lshl_add_u64 v[102:103], v[98:99], 2, s[6:7]
	s_waitcnt vmcnt(9)
	v_mov_b32_e32 v96, v179
	v_pk_mul_f32 v[94:95], v[94:95], v[96:97] op_sel_hi:[1,0]
	v_pk_mul_f32 v[92:93], v[92:93], v[96:97] op_sel_hi:[1,0]
	v_pk_mul_f32 v[90:91], v[90:91], v[96:97] op_sel_hi:[1,0]
	v_pk_mul_f32 v[88:89], v[88:89], v[96:97] op_sel_hi:[1,0]
	v_pk_mul_f32 v[86:87], v[86:87], v[96:97] op_sel_hi:[1,0]
	v_pk_mul_f32 v[84:85], v[84:85], v[96:97] op_sel_hi:[1,0]
	v_pk_mul_f32 v[104:105], v[82:83], v[96:97] op_sel_hi:[1,0]
	v_pk_mul_f32 v[96:97], v[80:81], v[96:97] op_sel_hi:[1,0]
	v_cvt_pk_bf16_f32 v80, v92, v93
	v_cvt_pk_bf16_f32 v81, v94, v95
	v_cvt_pk_bf16_f32 v82, v88, v89
	v_cvt_pk_bf16_f32 v83, v90, v91
	global_store_dwordx4 v[100:101], v[80:83], off
	s_nop 1
	v_cvt_pk_bf16_f32 v80, v84, v85
	v_cvt_pk_bf16_f32 v81, v86, v87
	v_cvt_pk_bf16_f32 v82, v96, v97
	v_cvt_pk_bf16_f32 v83, v104, v105
	global_store_dwordx4 v[100:101], v[80:83], off offset:256
	s_nop 0
	s_waitcnt vmcnt(10)
	v_mov_b32_e32 v80, v180
	v_pk_mul_f32 v[78:79], v[78:79], v[80:81] op_sel_hi:[1,0]
	v_subrev_u32_e32 v82, s52, v98
	v_ashrrev_i32_e32 v83, 31, v82
	v_lshlrev_b64 v[82:83], 12, v[82:83]
	v_lshl_add_u64 v[82:83], v[144:145], 0, v[82:83]
	v_pk_mul_f32 v[76:77], v[76:77], v[80:81] op_sel_hi:[1,0]
	v_pk_mul_f32 v[74:75], v[74:75], v[80:81] op_sel_hi:[1,0]
	v_pk_mul_f32 v[72:73], v[72:73], v[80:81] op_sel_hi:[1,0]
	v_pk_mul_f32 v[70:71], v[70:71], v[80:81] op_sel_hi:[1,0]
	v_pk_mul_f32 v[68:69], v[68:69], v[80:81] op_sel_hi:[1,0]
	v_pk_mul_f32 v[84:85], v[66:67], v[80:81] op_sel_hi:[1,0]
	v_pk_mul_f32 v[80:81], v[64:65], v[80:81] op_sel_hi:[1,0]
	v_cvt_pk_bf16_f32 v64, v76, v77
	v_cvt_pk_bf16_f32 v65, v78, v79
	v_cvt_pk_bf16_f32 v66, v72, v73
	v_cvt_pk_bf16_f32 v67, v74, v75
	global_store_dwordx4 v[82:83], v[64:67], off
	s_nop 1
	v_cvt_pk_bf16_f32 v64, v68, v69
	v_cvt_pk_bf16_f32 v65, v70, v71
	v_cvt_pk_bf16_f32 v66, v80, v81
	v_cvt_pk_bf16_f32 v67, v84, v85
	global_store_dwordx4 v[82:83], v[64:67], off offset:256
	s_nop 0
	s_waitcnt vmcnt(11)
	v_mov_b32_e32 v64, v181
	v_pk_mul_f32 v[62:63], v[62:63], v[64:65] op_sel_hi:[1,0]
	v_add_u32_e32 v66, 0x80, v142
	v_ashrrev_i32_e32 v67, 31, v66
	v_lshlrev_b64 v[66:67], 12, v[66:67]
	v_lshl_add_u64 v[66:67], v[144:145], 0, v[66:67]
	v_pk_mul_f32 v[60:61], v[60:61], v[64:65] op_sel_hi:[1,0]
	v_pk_mul_f32 v[58:59], v[58:59], v[64:65] op_sel_hi:[1,0]
	v_pk_mul_f32 v[56:57], v[56:57], v[64:65] op_sel_hi:[1,0]
	v_pk_mul_f32 v[54:55], v[54:55], v[64:65] op_sel_hi:[1,0]
	v_pk_mul_f32 v[52:53], v[52:53], v[64:65] op_sel_hi:[1,0]
	v_pk_mul_f32 v[68:69], v[50:51], v[64:65] op_sel_hi:[1,0]
	v_pk_mul_f32 v[64:65], v[48:49], v[64:65] op_sel_hi:[1,0]
	v_cvt_pk_bf16_f32 v48, v60, v61
	v_cvt_pk_bf16_f32 v49, v62, v63
	v_cvt_pk_bf16_f32 v50, v56, v57
	v_cvt_pk_bf16_f32 v51, v58, v59
	global_store_dwordx4 v[66:67], v[48:51], off
	s_nop 1
	v_cvt_pk_bf16_f32 v48, v52, v53
	v_cvt_pk_bf16_f32 v49, v54, v55
	v_cvt_pk_bf16_f32 v50, v64, v65
	v_cvt_pk_bf16_f32 v51, v68, v69
	global_store_dwordx4 v[66:67], v[48:51], off offset:256
	s_nop 0
	s_waitcnt vmcnt(12)
	v_mov_b32_e32 v48, v182
	v_pk_mul_f32 v[46:47], v[46:47], v[48:49] op_sel_hi:[1,0]
	v_add_u32_e32 v50, 0x90, v142
	v_ashrrev_i32_e32 v51, 31, v50
	v_lshlrev_b64 v[50:51], 12, v[50:51]
	v_lshl_add_u64 v[50:51], v[144:145], 0, v[50:51]
	v_pk_mul_f32 v[44:45], v[44:45], v[48:49] op_sel_hi:[1,0]
	v_pk_mul_f32 v[42:43], v[42:43], v[48:49] op_sel_hi:[1,0]
	v_pk_mul_f32 v[40:41], v[40:41], v[48:49] op_sel_hi:[1,0]
	v_pk_mul_f32 v[38:39], v[38:39], v[48:49] op_sel_hi:[1,0]
	v_pk_mul_f32 v[36:37], v[36:37], v[48:49] op_sel_hi:[1,0]
	v_pk_mul_f32 v[52:53], v[34:35], v[48:49] op_sel_hi:[1,0]
	v_pk_mul_f32 v[48:49], v[32:33], v[48:49] op_sel_hi:[1,0]
	v_cvt_pk_bf16_f32 v32, v44, v45
	v_cvt_pk_bf16_f32 v33, v46, v47
	v_cvt_pk_bf16_f32 v34, v40, v41
	v_cvt_pk_bf16_f32 v35, v42, v43
	global_store_dwordx4 v[50:51], v[32:35], off
	s_nop 1
	v_cvt_pk_bf16_f32 v32, v36, v37
	v_cvt_pk_bf16_f32 v33, v38, v39
	v_cvt_pk_bf16_f32 v34, v48, v49
	v_cvt_pk_bf16_f32 v35, v52, v53
	global_store_dwordx4 v[50:51], v[32:35], off offset:256
	s_nop 0
	s_waitcnt vmcnt(13)
	v_mov_b32_e32 v32, v183
	v_pk_mul_f32 v[30:31], v[30:31], v[32:33] op_sel_hi:[1,0]
	v_add_u32_e32 v34, 0xa0, v142
	v_ashrrev_i32_e32 v35, 31, v34
	v_lshlrev_b64 v[34:35], 12, v[34:35]
	v_lshl_add_u64 v[34:35], v[144:145], 0, v[34:35]
	v_pk_mul_f32 v[28:29], v[28:29], v[32:33] op_sel_hi:[1,0]
	v_pk_mul_f32 v[26:27], v[26:27], v[32:33] op_sel_hi:[1,0]
	v_pk_mul_f32 v[24:25], v[24:25], v[32:33] op_sel_hi:[1,0]
	v_pk_mul_f32 v[22:23], v[22:23], v[32:33] op_sel_hi:[1,0]
	v_pk_mul_f32 v[20:21], v[20:21], v[32:33] op_sel_hi:[1,0]
	v_pk_mul_f32 v[36:37], v[18:19], v[32:33] op_sel_hi:[1,0]
	v_pk_mul_f32 v[32:33], v[16:17], v[32:33] op_sel_hi:[1,0]
	v_cvt_pk_bf16_f32 v16, v28, v29
	v_cvt_pk_bf16_f32 v17, v30, v31
	v_cvt_pk_bf16_f32 v18, v24, v25
	v_cvt_pk_bf16_f32 v19, v26, v27
	global_store_dwordx4 v[34:35], v[16:19], off
	s_nop 1
	v_cvt_pk_bf16_f32 v16, v20, v21
	v_cvt_pk_bf16_f32 v17, v22, v23
	v_cvt_pk_bf16_f32 v18, v32, v33
	v_cvt_pk_bf16_f32 v19, v36, v37
	global_store_dwordx4 v[34:35], v[16:19], off offset:256
	s_nop 0
	s_waitcnt vmcnt(14)
	v_mov_b32_e32 v16, v184
	v_pk_mul_f32 v[14:15], v[14:15], v[16:17] op_sel_hi:[1,0]
	v_add_u32_e32 v18, 0xb0, v142
	v_ashrrev_i32_e32 v19, 31, v18
	v_lshlrev_b64 v[18:19], 12, v[18:19]
	v_lshl_add_u64 v[18:19], v[144:145], 0, v[18:19]
	v_pk_mul_f32 v[12:13], v[12:13], v[16:17] op_sel_hi:[1,0]
	v_pk_mul_f32 v[10:11], v[10:11], v[16:17] op_sel_hi:[1,0]
	v_pk_mul_f32 v[8:9], v[8:9], v[16:17] op_sel_hi:[1,0]
	v_pk_mul_f32 v[6:7], v[6:7], v[16:17] op_sel_hi:[1,0]
	v_pk_mul_f32 v[4:5], v[4:5], v[16:17] op_sel_hi:[1,0]
	v_pk_mul_f32 v[20:21], v[2:3], v[16:17] op_sel_hi:[1,0]
	v_pk_mul_f32 v[16:17], v[0:1], v[16:17] op_sel_hi:[1,0]
	v_cvt_pk_bf16_f32 v0, v12, v13
	v_cvt_pk_bf16_f32 v1, v14, v15
	v_cvt_pk_bf16_f32 v2, v8, v9
	v_cvt_pk_bf16_f32 v3, v10, v11
	global_store_dwordx4 v[18:19], v[0:3], off
	s_nop 1
	v_cvt_pk_bf16_f32 v0, v4, v5
	v_cvt_pk_bf16_f32 v1, v6, v7
	v_cvt_pk_bf16_f32 v2, v16, v17
	v_cvt_pk_bf16_f32 v3, v20, v21
	global_store_dwordx4 v[18:19], v[0:3], off offset:256
	s_cbranch_vccnz .LBB0_1171
	s_andn2_b64 vcc, exec, s[0:1]
	s_cbranch_vccnz .LBB0_1170
	s_barrier
	s_branch .LBB0_1170
